# tail barriers (after up GEMM and MoE2): the workgroups busy to the end also convert one item per wave in the barrier shadow, taken off the lockstep streams
# speedup vs baseline: 1.0020x; 1.0020x over previous
.Lcvt_t3:
	s_cmp_eq_u32 s31, 3
	s_cbranch_scc0 .Lcvt_t10
	s_mov_b32 s24, s62
	s_sub_i32 s27, s63, 208
	s_cmp_lt_i32 s27, 0
	s_cbranch_scc1 .Lcvt_t3b
	s_mov_b32 s26, 1
	s_movk_i32 s30, 5040
	s_movk_i32 s4, 5376
	s_branch .Lcvt_go
.Lcvt_t3b:
	s_mov_b32 s27, s63
	s_mov_b32 s26, 1
	s_movk_i32 s30, 5376
	s_movk_i32 s4, 6832
	s_branch .Lcvt_go
.Lcvt_t10:
	s_cmp_eq_u32 s31, 10
	s_cbranch_scc0 .Lcvt_lock
	s_cmp_ge_u32 s62, 3
	s_cbranch_scc1 .Lcvt_ret
	s_add_i32 s24, s62, 1
	s_sub_i32 s27, s63, 136
	s_cmp_lt_i32 s27, 0
	s_cbranch_scc1 .Lcvt_t10b
	s_mov_b32 s26, 4
	s_movk_i32 s30, 6832
	s_movk_i32 s4, 10192
	s_branch .Lcvt_go
.Lcvt_t10b:
	s_mov_b32 s27, s63
	s_mov_b32 s26, 1
	s_movk_i32 s30, 10192
	s_movk_i32 s4, 11144

.Lcvt_lk_c:
	s_mov_b32 s26, 2535
	s_mov_b32 s4, 17744
	s_cmp_eq_u32 s27, 1
	s_cselect_b32 s26, 1679, s26
	s_cselect_b32 s4, 13432, s4
	s_cmp_eq_u32 s27, 2
	s_cselect_b32 s26, 1679, s26
	s_cselect_b32 s4, 13432, s4
	s_cmp_eq_u32 s27, 3
	s_cselect_b32 s26, 2309, s26
	s_cselect_b32 s4, 18472, s4
	s_mul_i32 s30, s24, s26
	s_add_i32 s24, s30, s26
	s_min_u32 s4, s4, s24
	s_mul_i32 s26, s80, 7
	s_add_i32 s26, s26, s25
	s_add_i32 s26, s26, -1
	s_add_i32 s30, s30, s26
	s_mov_b32 s26, 2
	s_movk_i32 s25, 0x700
.Lcvt_item:
	s_cmp_ge_u32 s30, s4
	s_cbranch_scc1 .Lcvt_ret
	s_mov_b32 s6, s27
	s_mov_b32 s5, s30
	s_cmp_eq_u32 s25, 1
	s_cbranch_scc1 .Lcvt_dec
	s_cmp_eq_u32 s27, 3
	s_cbranch_scc1 .Lcvt_m3
	s_mov_b32 s24, 6832
	s_cmp_eq_u32 s27, 0
	s_cselect_b32 s24, s24, 11144
	s_add_i32 s5, s5, s24
	s_branch .Lcvt_dec
.Lcvt_m3:
	s_cmp_lt_u32 s5, 5040
	s_cbranch_scc1 .Lcvt_dec
	s_add_i32 s5, s5, 6104
